# SwiGLU epilogue re-emitted: packed mul/add, rstd broadcast via op_sel, 8 chains interleaved (no s_nop), one address per half
# speedup vs baseline: 1.0044x; 1.0010x over previous
; __device__ __forceinline__ unsigned cvt_pk_bf16(float lo, float hi) { const f32x2_t v = {lo, hi}; const bf16x2_t b = __builtin_convertvector(v, bf16x2_t); return __builtin_bit_cast(unsigned, b); }
;     __device__ __forceinline__ void operator()(const f32x4 (&acc)[2][2][4][2], const Unit& u, int wr, int wc, int fr, int fq, int ui) const {
;     ...
;         for (int ai = 0; ai < 2; ++ai)
; #pragma unroll
;             for (int m = 0; m < 4; ++m) rs[ai][m] = rtab[ui * 256 + ai * HALF + wr * 64 + m * 16 + fr];
; #pragma unroll
;         for (int ai = 0; ai < 2; ++ai)
; #pragma unroll
;             for (int m = 0; m < 4; ++m) {
;                 const float r = rs[ai][m]; const int row = u.pm * BM + ai * HALF + wr * 64 + m * 16 + fr;
;                 float g[8], v[8], e[8];
; #pragma unroll
;                 for (int n = 0; n < 2; ++n)
; #pragma unroll
;                     for (int i = 0; i < 4; ++i) { g[n * 4 + i] = fmaf(acc[ai][0][m][n][i], r, bg[n][i]); v[n * 4 + i] = fmaf(acc[ai][1][m][n][i], r, bu[n][i]); }
; #pragma unroll
;                 for (int i = 0; i < 8; ++i) e[i] = __builtin_amdgcn_exp2f(g[i] * (-LOG2E));
; #pragma unroll
;                 for (int i = 0; i < 8; ++i) e[i] = __builtin_amdgcn_rcpf(1.0f + e[i]);
; #pragma unroll
;                 for (int i = 0; i < 8; ++i) e[i] = (g[i] * e[i]) * v[i];
;                 u32x4 w; w.x = cvt_pk_bf16(e[0], e[1]); w.y = cvt_pk_bf16(e[2], e[3]); w.z = cvt_pk_bf16(e[4], e[5]); w.w = cvt_pk_bf16(e[6], e[7]);
;                 *(u32x4*)(act + ((size_t)((row >> 8) * (F / 64) + (jcol >> 6)) * 256 + (row & 255)) * 64 + (jcol & 63)) = w;
.LBB0_249:
	v_lshl_add_u32 v162, s56, 8, v171
	v_lshl_add_u32 v162, v162, 2, 0
	v_lshl_add_u32 v84, s56, 10, v179
	v_add_u32_e32 v162, 0x22000, v162
	ds_read_b128 v[96:99], v84
	ds_read_b128 v[80:83], v84 offset:16
	ds_read_b128 v[100:103], v84 offset:512
	ds_read_b128 v[84:87], v84 offset:528
	ds_read2_b32 v[166:167], v162 offset1:16
	ds_read2_b32 v[176:177], v162 offset0:32 offset1:48
	ds_read2_b32 v[164:165], v162 offset0:128 offset1:144
	ds_read2_b32 v[162:163], v162 offset0:160 offset1:176
	s_lshl_b32 s11, s55, 8
	s_waitcnt lgkmcnt(0)
	v_mov_b32_e32 v222, 0xbfb8aa3b
	v_mov_b32_e32 v224, 1.0
	s_lshl_b32 s9, s57, 7
	s_add_i32 s16, s11, s49
	s_or_b32 s9, s9, s50
	s_ashr_i32 s16, s16, 8
	s_ashr_i32 s9, s9, 6
	s_mulk_i32 s16, 0x58
	s_add_i32 s16, s16, s9
	s_ashr_i32 s17, s16, 31
	s_lshl_b64 s[16:17], s[16:17], 15
	s_add_u32 s16, s16, 0x1000
	s_addc_u32 s17, s17, 0
	v_lshl_add_u64 v[214:215], v[154:155], 0, s[16:17]
	v_lshl_add_u64 v[214:215], v[214:215], 0, v[128:129]
	s_add_i32 s11, s11, s53
	s_ashr_i32 s11, s11, 8
	s_mulk_i32 s11, 0x58
	s_add_i32 s16, s11, s9
	s_ashr_i32 s17, s16, 31
	s_lshl_b64 s[16:17], s[16:17], 15
	s_add_u32 s16, s16, 0x1000
	s_addc_u32 s17, s17, 0
	v_lshl_add_u64 v[216:217], v[156:157], 0, s[16:17]
	v_lshl_add_u64 v[216:217], v[216:217], 0, v[128:129]
	s_mov_b64 s[16:17], -1
	s_movk_i32 s18, 0x1000
	s_mov_b32 s65, s67
	v_pk_fma_f32 v[142:143], v[142:143], v[166:167], v[96:97] op_sel_hi:[1,0,1]
	v_pk_fma_f32 v[144:145], v[144:145], v[166:167], v[98:99] op_sel_hi:[1,0,1]
	v_pk_fma_f32 v[134:135], v[134:135], v[166:167], v[80:81] op_sel_hi:[1,0,1]
	v_pk_fma_f32 v[136:137], v[136:137], v[166:167], v[82:83] op_sel_hi:[1,0,1]
	v_pk_mul_f32 v[198:199], v[142:143], v[222:223] op_sel_hi:[1,0]
	v_pk_mul_f32 v[200:201], v[144:145], v[222:223] op_sel_hi:[1,0]
	v_pk_mul_f32 v[202:203], v[134:135], v[222:223] op_sel_hi:[1,0]
	v_pk_mul_f32 v[204:205], v[136:137], v[222:223] op_sel_hi:[1,0]
	v_pk_fma_f32 v[138:139], v[138:139], v[166:167], v[100:101] op_sel_hi:[1,0,1]
	v_pk_fma_f32 v[140:141], v[140:141], v[166:167], v[102:103] op_sel_hi:[1,0,1]
	v_pk_fma_f32 v[130:131], v[130:131], v[166:167], v[84:85] op_sel_hi:[1,0,1]
	v_pk_fma_f32 v[132:133], v[132:133], v[166:167], v[86:87] op_sel_hi:[1,0,1]
	v_exp_f32_e32 v198, v198
	v_exp_f32_e32 v199, v199
	v_exp_f32_e32 v200, v200
	v_exp_f32_e32 v201, v201
	v_exp_f32_e32 v202, v202
	v_exp_f32_e32 v203, v203
	v_exp_f32_e32 v204, v204
	v_exp_f32_e32 v205, v205
	v_pk_add_f32 v[198:199], v[198:199], v[224:225] op_sel_hi:[1,0]
	v_pk_add_f32 v[200:201], v[200:201], v[224:225] op_sel_hi:[1,0]
	v_pk_add_f32 v[202:203], v[202:203], v[224:225] op_sel_hi:[1,0]
	v_pk_add_f32 v[204:205], v[204:205], v[224:225] op_sel_hi:[1,0]
	v_rcp_f32_e32 v198, v198
	v_rcp_f32_e32 v199, v199
	v_rcp_f32_e32 v200, v200
	v_rcp_f32_e32 v201, v201
	v_rcp_f32_e32 v202, v202
	v_rcp_f32_e32 v203, v203
	v_rcp_f32_e32 v204, v204
	v_rcp_f32_e32 v205, v205
	v_pk_mul_f32 v[142:143], v[142:143], v[198:199]
	v_pk_mul_f32 v[144:145], v[144:145], v[200:201]
	v_pk_mul_f32 v[134:135], v[134:135], v[202:203]
	v_pk_mul_f32 v[136:137], v[136:137], v[204:205]
	v_pk_mul_f32 v[142:143], v[138:139], v[142:143]
	v_pk_mul_f32 v[144:145], v[140:141], v[144:145]
	v_pk_mul_f32 v[134:135], v[130:131], v[134:135]
	v_pk_mul_f32 v[136:137], v[132:133], v[136:137]
	v_cvt_pk_bf16_f32 v206, v142, v143
	v_cvt_pk_bf16_f32 v207, v144, v145
	v_cvt_pk_bf16_f32 v208, v134, v135
	v_cvt_pk_bf16_f32 v209, v136, v137
	global_store_dwordx4 v[214:215], v[206:209], off offset:-4096
	v_pk_fma_f32 v[124:125], v[124:125], v[166:167], v[96:97] op_sel:[0,1,0]
	v_pk_fma_f32 v[126:127], v[126:127], v[166:167], v[98:99] op_sel:[0,1,0]
	v_pk_fma_f32 v[116:117], v[116:117], v[166:167], v[80:81] op_sel:[0,1,0]
	v_pk_fma_f32 v[118:119], v[118:119], v[166:167], v[82:83] op_sel:[0,1,0]
	v_pk_mul_f32 v[198:199], v[124:125], v[222:223] op_sel_hi:[1,0]
	v_pk_mul_f32 v[200:201], v[126:127], v[222:223] op_sel_hi:[1,0]
	v_pk_mul_f32 v[202:203], v[116:117], v[222:223] op_sel_hi:[1,0]
	v_pk_mul_f32 v[204:205], v[118:119], v[222:223] op_sel_hi:[1,0]
	v_pk_fma_f32 v[120:121], v[120:121], v[166:167], v[100:101] op_sel:[0,1,0]
	v_pk_fma_f32 v[122:123], v[122:123], v[166:167], v[102:103] op_sel:[0,1,0]
	v_pk_fma_f32 v[112:113], v[112:113], v[166:167], v[84:85] op_sel:[0,1,0]
	v_pk_fma_f32 v[114:115], v[114:115], v[166:167], v[86:87] op_sel:[0,1,0]
	v_exp_f32_e32 v198, v198
	v_exp_f32_e32 v199, v199
	v_exp_f32_e32 v200, v200
	v_exp_f32_e32 v201, v201
	v_exp_f32_e32 v202, v202
	v_exp_f32_e32 v203, v203
	v_exp_f32_e32 v204, v204
	v_exp_f32_e32 v205, v205
	v_pk_add_f32 v[198:199], v[198:199], v[224:225] op_sel_hi:[1,0]
	v_pk_add_f32 v[200:201], v[200:201], v[224:225] op_sel_hi:[1,0]
	v_pk_add_f32 v[202:203], v[202:203], v[224:225] op_sel_hi:[1,0]
	v_pk_add_f32 v[204:205], v[204:205], v[224:225] op_sel_hi:[1,0]
	v_rcp_f32_e32 v198, v198
	v_rcp_f32_e32 v199, v199
	v_rcp_f32_e32 v200, v200
	v_rcp_f32_e32 v201, v201
	v_rcp_f32_e32 v202, v202
	v_rcp_f32_e32 v203, v203
	v_rcp_f32_e32 v204, v204
	v_rcp_f32_e32 v205, v205
	v_pk_mul_f32 v[124:125], v[124:125], v[198:199]
	v_pk_mul_f32 v[126:127], v[126:127], v[200:201]
	v_pk_mul_f32 v[116:117], v[116:117], v[202:203]
	v_pk_mul_f32 v[118:119], v[118:119], v[204:205]
	v_pk_mul_f32 v[124:125], v[120:121], v[124:125]
	v_pk_mul_f32 v[126:127], v[122:123], v[126:127]
	v_pk_mul_f32 v[116:117], v[112:113], v[116:117]
	v_pk_mul_f32 v[118:119], v[114:115], v[118:119]
	v_cvt_pk_bf16_f32 v210, v124, v125
	v_cvt_pk_bf16_f32 v211, v126, v127
	v_cvt_pk_bf16_f32 v212, v116, v117
	v_cvt_pk_bf16_f32 v213, v118, v119
	global_store_dwordx4 v[214:215], v[210:213], off offset:-2048
; __device__ __forceinline__ unsigned cvt_pk_bf16(float lo, float hi) { const f32x2_t v = {lo, hi}; const bf16x2_t b = __builtin_convertvector(v, bf16x2_t); return __builtin_bit_cast(unsigned, b); }
;     __device__ __forceinline__ void operator()(const f32x4 (&acc)[2][2][4][2], const Unit& u, int wr, int wc, int fr, int fq, int ui) const {
;     ...
;                 for (int n = 0; n < 2; ++n)
; #pragma unroll
;                     for (int i = 0; i < 4; ++i) { g[n * 4 + i] = fmaf(acc[ai][0][m][n][i], r, bg[n][i]); v[n * 4 + i] = fmaf(acc[ai][1][m][n][i], r, bu[n][i]); }
; #pragma unroll
;                 for (int i = 0; i < 8; ++i) e[i] = __builtin_amdgcn_exp2f(g[i] * (-LOG2E));
; #pragma unroll
;                 for (int i = 0; i < 8; ++i) e[i] = __builtin_amdgcn_rcpf(1.0f + e[i]);
; #pragma unroll
;                 for (int i = 0; i < 8; ++i) e[i] = (g[i] * e[i]) * v[i];
;                 u32x4 w; w.x = cvt_pk_bf16(e[0], e[1]); w.y = cvt_pk_bf16(e[2], e[3]); w.z = cvt_pk_bf16(e[4], e[5]); w.w = cvt_pk_bf16(e[6], e[7]);
;                 *(u32x4*)(act + ((size_t)((row >> 8) * (F / 64) + (jcol >> 6)) * 256 + (row & 255)) * 64 + (jcol & 63)) = w;
	v_pk_fma_f32 v[108:109], v[108:109], v[176:177], v[96:97] op_sel_hi:[1,0,1]
	v_pk_fma_f32 v[110:111], v[110:111], v[176:177], v[98:99] op_sel_hi:[1,0,1]
	v_pk_fma_f32 v[92:93], v[92:93], v[176:177], v[80:81] op_sel_hi:[1,0,1]
	v_pk_fma_f32 v[94:95], v[94:95], v[176:177], v[82:83] op_sel_hi:[1,0,1]
	v_pk_mul_f32 v[198:199], v[108:109], v[222:223] op_sel_hi:[1,0]
	v_pk_mul_f32 v[200:201], v[110:111], v[222:223] op_sel_hi:[1,0]
	v_pk_mul_f32 v[202:203], v[92:93], v[222:223] op_sel_hi:[1,0]
	v_pk_mul_f32 v[204:205], v[94:95], v[222:223] op_sel_hi:[1,0]
	v_pk_fma_f32 v[104:105], v[104:105], v[176:177], v[100:101] op_sel_hi:[1,0,1]
	v_pk_fma_f32 v[106:107], v[106:107], v[176:177], v[102:103] op_sel_hi:[1,0,1]
	v_pk_fma_f32 v[88:89], v[88:89], v[176:177], v[84:85] op_sel_hi:[1,0,1]
	v_pk_fma_f32 v[90:91], v[90:91], v[176:177], v[86:87] op_sel_hi:[1,0,1]
	v_exp_f32_e32 v198, v198
	v_exp_f32_e32 v199, v199
	v_exp_f32_e32 v200, v200
	v_exp_f32_e32 v201, v201
	v_exp_f32_e32 v202, v202
	v_exp_f32_e32 v203, v203
	v_exp_f32_e32 v204, v204
	v_exp_f32_e32 v205, v205
	v_pk_add_f32 v[198:199], v[198:199], v[224:225] op_sel_hi:[1,0]
	v_pk_add_f32 v[200:201], v[200:201], v[224:225] op_sel_hi:[1,0]
	v_pk_add_f32 v[202:203], v[202:203], v[224:225] op_sel_hi:[1,0]
	v_pk_add_f32 v[204:205], v[204:205], v[224:225] op_sel_hi:[1,0]
	v_rcp_f32_e32 v198, v198
	v_rcp_f32_e32 v199, v199
	v_rcp_f32_e32 v200, v200
	v_rcp_f32_e32 v201, v201
	v_rcp_f32_e32 v202, v202
	v_rcp_f32_e32 v203, v203
	v_rcp_f32_e32 v204, v204
	v_rcp_f32_e32 v205, v205
	v_pk_mul_f32 v[108:109], v[108:109], v[198:199]
	v_pk_mul_f32 v[110:111], v[110:111], v[200:201]
	v_pk_mul_f32 v[92:93], v[92:93], v[202:203]
	v_pk_mul_f32 v[94:95], v[94:95], v[204:205]
	v_pk_mul_f32 v[108:109], v[104:105], v[108:109]
	v_pk_mul_f32 v[110:111], v[106:107], v[110:111]
	v_pk_mul_f32 v[92:93], v[88:89], v[92:93]
	v_pk_mul_f32 v[94:95], v[90:91], v[94:95]
	v_cvt_pk_bf16_f32 v206, v108, v109
	v_cvt_pk_bf16_f32 v207, v110, v111
	v_cvt_pk_bf16_f32 v208, v92, v93
	v_cvt_pk_bf16_f32 v209, v94, v95
	global_store_dwordx4 v[214:215], v[206:209], off
	v_pk_fma_f32 v[76:77], v[76:77], v[176:177], v[96:97] op_sel:[0,1,0]
	v_pk_fma_f32 v[78:79], v[78:79], v[176:177], v[98:99] op_sel:[0,1,0]
	v_pk_fma_f32 v[68:69], v[68:69], v[176:177], v[80:81] op_sel:[0,1,0]
	v_pk_fma_f32 v[70:71], v[70:71], v[176:177], v[82:83] op_sel:[0,1,0]
	v_pk_mul_f32 v[198:199], v[76:77], v[222:223] op_sel_hi:[1,0]
	v_pk_mul_f32 v[200:201], v[78:79], v[222:223] op_sel_hi:[1,0]
	v_pk_mul_f32 v[202:203], v[68:69], v[222:223] op_sel_hi:[1,0]
	v_pk_mul_f32 v[204:205], v[70:71], v[222:223] op_sel_hi:[1,0]
	v_pk_fma_f32 v[72:73], v[72:73], v[176:177], v[100:101] op_sel:[0,1,0]
	v_pk_fma_f32 v[74:75], v[74:75], v[176:177], v[102:103] op_sel:[0,1,0]
	v_pk_fma_f32 v[64:65], v[64:65], v[176:177], v[84:85] op_sel:[0,1,0]
	v_pk_fma_f32 v[66:67], v[66:67], v[176:177], v[86:87] op_sel:[0,1,0]
	v_exp_f32_e32 v198, v198
	v_exp_f32_e32 v199, v199
	v_exp_f32_e32 v200, v200
	v_exp_f32_e32 v201, v201
	v_exp_f32_e32 v202, v202
	v_exp_f32_e32 v203, v203
	v_exp_f32_e32 v204, v204
	v_exp_f32_e32 v205, v205
	v_pk_add_f32 v[198:199], v[198:199], v[224:225] op_sel_hi:[1,0]
	v_pk_add_f32 v[200:201], v[200:201], v[224:225] op_sel_hi:[1,0]
	v_pk_add_f32 v[202:203], v[202:203], v[224:225] op_sel_hi:[1,0]
	v_pk_add_f32 v[204:205], v[204:205], v[224:225] op_sel_hi:[1,0]
	v_rcp_f32_e32 v198, v198
	v_rcp_f32_e32 v199, v199
	v_rcp_f32_e32 v200, v200
	v_rcp_f32_e32 v201, v201
	v_rcp_f32_e32 v202, v202
	v_rcp_f32_e32 v203, v203
	v_rcp_f32_e32 v204, v204
	v_rcp_f32_e32 v205, v205
	v_pk_mul_f32 v[76:77], v[76:77], v[198:199]
	v_pk_mul_f32 v[78:79], v[78:79], v[200:201]
	v_pk_mul_f32 v[68:69], v[68:69], v[202:203]
	v_pk_mul_f32 v[70:71], v[70:71], v[204:205]
	v_pk_mul_f32 v[76:77], v[72:73], v[76:77]
	v_pk_mul_f32 v[78:79], v[74:75], v[78:79]
	v_pk_mul_f32 v[68:69], v[64:65], v[68:69]
	v_pk_mul_f32 v[70:71], v[66:67], v[70:71]
	v_cvt_pk_bf16_f32 v210, v76, v77
	v_cvt_pk_bf16_f32 v211, v78, v79
	v_cvt_pk_bf16_f32 v212, v68, v69
	v_cvt_pk_bf16_f32 v213, v70, v71
	global_store_dwordx4 v[214:215], v[210:213], off offset:2048
	v_pk_fma_f32 v[60:61], v[60:61], v[164:165], v[96:97] op_sel_hi:[1,0,1]
	v_pk_fma_f32 v[62:63], v[62:63], v[164:165], v[98:99] op_sel_hi:[1,0,1]
	v_pk_fma_f32 v[52:53], v[52:53], v[164:165], v[80:81] op_sel_hi:[1,0,1]
	v_pk_fma_f32 v[54:55], v[54:55], v[164:165], v[82:83] op_sel_hi:[1,0,1]
	v_pk_mul_f32 v[198:199], v[60:61], v[222:223] op_sel_hi:[1,0]
	v_pk_mul_f32 v[200:201], v[62:63], v[222:223] op_sel_hi:[1,0]
	v_pk_mul_f32 v[202:203], v[52:53], v[222:223] op_sel_hi:[1,0]
	v_pk_mul_f32 v[204:205], v[54:55], v[222:223] op_sel_hi:[1,0]
	v_pk_fma_f32 v[56:57], v[56:57], v[164:165], v[100:101] op_sel_hi:[1,0,1]
	v_pk_fma_f32 v[58:59], v[58:59], v[164:165], v[102:103] op_sel_hi:[1,0,1]
	v_pk_fma_f32 v[48:49], v[48:49], v[164:165], v[84:85] op_sel_hi:[1,0,1]
	v_pk_fma_f32 v[50:51], v[50:51], v[164:165], v[86:87] op_sel_hi:[1,0,1]
	v_exp_f32_e32 v198, v198
	v_exp_f32_e32 v199, v199
	v_exp_f32_e32 v200, v200
	v_exp_f32_e32 v201, v201
	v_exp_f32_e32 v202, v202
	v_exp_f32_e32 v203, v203
	v_exp_f32_e32 v204, v204
	v_exp_f32_e32 v205, v205
	v_pk_add_f32 v[198:199], v[198:199], v[224:225] op_sel_hi:[1,0]
	v_pk_add_f32 v[200:201], v[200:201], v[224:225] op_sel_hi:[1,0]
	v_pk_add_f32 v[202:203], v[202:203], v[224:225] op_sel_hi:[1,0]
	v_pk_add_f32 v[204:205], v[204:205], v[224:225] op_sel_hi:[1,0]
	v_rcp_f32_e32 v198, v198
	v_rcp_f32_e32 v199, v199
	v_rcp_f32_e32 v200, v200
	v_rcp_f32_e32 v201, v201
	v_rcp_f32_e32 v202, v202
	v_rcp_f32_e32 v203, v203
	v_rcp_f32_e32 v204, v204
; __device__ __forceinline__ unsigned cvt_pk_bf16(float lo, float hi) { const f32x2_t v = {lo, hi}; const bf16x2_t b = __builtin_convertvector(v, bf16x2_t); return __builtin_bit_cast(unsigned, b); }
; #define PG8_BAR __builtin_amdgcn_s_barrier()
;     __device__ __forceinline__ void operator()(const f32x4 (&acc)[2][2][4][2], const Unit& u, int wr, int wc, int fr, int fq, int ui) const {
;     ...
;                 for (int n = 0; n < 2; ++n)
; #pragma unroll
;                     for (int i = 0; i < 4; ++i) { g[n * 4 + i] = fmaf(acc[ai][0][m][n][i], r, bg[n][i]); v[n * 4 + i] = fmaf(acc[ai][1][m][n][i], r, bu[n][i]); }
; #pragma unroll
;                 for (int i = 0; i < 8; ++i) e[i] = __builtin_amdgcn_exp2f(g[i] * (-LOG2E));
; #pragma unroll
;                 for (int i = 0; i < 8; ++i) e[i] = __builtin_amdgcn_rcpf(1.0f + e[i]);
; #pragma unroll
;                 for (int i = 0; i < 8; ++i) e[i] = (g[i] * e[i]) * v[i];
;                 u32x4 w; w.x = cvt_pk_bf16(e[0], e[1]); w.y = cvt_pk_bf16(e[2], e[3]); w.z = cvt_pk_bf16(e[4], e[5]); w.w = cvt_pk_bf16(e[6], e[7]);
;                 *(u32x4*)(act + ((size_t)((row >> 8) * (F / 64) + (jcol >> 6)) * 256 + (row & 255)) * 64 + (jcol & 63)) = w;
; template <class Epi, class Sched, bool ALIGN_EPI>
; __device__ __forceinline__ void gemm_phase(PG8_LAS unsigned char* lds, const Gemm g, const Sched& S, const Epi& E, const int tid) {
;     ...
;         }
;         if constexpr (ALIGN_EPI) { if (wr == 0) PG8_BAR; }
;         E(acc, cur, wr, wc, fr, fq, ui); S.done(cur);
;         if (!has_next) break;
; #pragma unroll
;         for (int a = 0; a < 2; ++a)
; #pragma unroll
;             for (int b = 0; b < 2; ++b)
; #pragma unroll
;                 for (int m = 0; m < 4; ++m)
; #pragma unroll
;                     for (int n = 0; n < 2; ++n) acc[a][b][m][n] = (f32x4){0.f, 0.f, 0.f, 0.f};
;         cur = nxt; cA = nA; cB = nB; ++ui;
;         if constexpr (ALIGN_EPI) { if (wr == 1) PG8_BAR; }
	v_rcp_f32_e32 v205, v205
	v_pk_mul_f32 v[60:61], v[60:61], v[198:199]
	v_pk_mul_f32 v[62:63], v[62:63], v[200:201]
	v_pk_mul_f32 v[52:53], v[52:53], v[202:203]
	v_pk_mul_f32 v[54:55], v[54:55], v[204:205]
	v_pk_mul_f32 v[60:61], v[56:57], v[60:61]
	v_pk_mul_f32 v[62:63], v[58:59], v[62:63]
	v_pk_mul_f32 v[52:53], v[48:49], v[52:53]
	v_pk_mul_f32 v[54:55], v[50:51], v[54:55]
	v_cvt_pk_bf16_f32 v206, v60, v61
	v_cvt_pk_bf16_f32 v207, v62, v63
	v_cvt_pk_bf16_f32 v208, v52, v53
	v_cvt_pk_bf16_f32 v209, v54, v55
	global_store_dwordx4 v[216:217], v[206:209], off offset:-4096
	v_pk_fma_f32 v[44:45], v[44:45], v[164:165], v[96:97] op_sel:[0,1,0]
	v_pk_fma_f32 v[46:47], v[46:47], v[164:165], v[98:99] op_sel:[0,1,0]
	v_pk_fma_f32 v[36:37], v[36:37], v[164:165], v[80:81] op_sel:[0,1,0]
	v_pk_fma_f32 v[38:39], v[38:39], v[164:165], v[82:83] op_sel:[0,1,0]
	v_pk_mul_f32 v[198:199], v[44:45], v[222:223] op_sel_hi:[1,0]
	v_pk_mul_f32 v[200:201], v[46:47], v[222:223] op_sel_hi:[1,0]
	v_pk_mul_f32 v[202:203], v[36:37], v[222:223] op_sel_hi:[1,0]
	v_pk_mul_f32 v[204:205], v[38:39], v[222:223] op_sel_hi:[1,0]
	v_pk_fma_f32 v[40:41], v[40:41], v[164:165], v[100:101] op_sel:[0,1,0]
	v_pk_fma_f32 v[42:43], v[42:43], v[164:165], v[102:103] op_sel:[0,1,0]
	v_pk_fma_f32 v[32:33], v[32:33], v[164:165], v[84:85] op_sel:[0,1,0]
	v_pk_fma_f32 v[34:35], v[34:35], v[164:165], v[86:87] op_sel:[0,1,0]
	v_exp_f32_e32 v198, v198
	v_exp_f32_e32 v199, v199
	v_exp_f32_e32 v200, v200
	v_exp_f32_e32 v201, v201
	v_exp_f32_e32 v202, v202
	v_exp_f32_e32 v203, v203
	v_exp_f32_e32 v204, v204
	v_exp_f32_e32 v205, v205
	v_pk_add_f32 v[198:199], v[198:199], v[224:225] op_sel_hi:[1,0]
	v_pk_add_f32 v[200:201], v[200:201], v[224:225] op_sel_hi:[1,0]
	v_pk_add_f32 v[202:203], v[202:203], v[224:225] op_sel_hi:[1,0]
	v_pk_add_f32 v[204:205], v[204:205], v[224:225] op_sel_hi:[1,0]
	v_rcp_f32_e32 v198, v198
	v_rcp_f32_e32 v199, v199
	v_rcp_f32_e32 v200, v200
	v_rcp_f32_e32 v201, v201
	v_rcp_f32_e32 v202, v202
	v_rcp_f32_e32 v203, v203
	v_rcp_f32_e32 v204, v204
	v_rcp_f32_e32 v205, v205
	v_pk_mul_f32 v[44:45], v[44:45], v[198:199]
	v_pk_mul_f32 v[46:47], v[46:47], v[200:201]
	v_pk_mul_f32 v[36:37], v[36:37], v[202:203]
	v_pk_mul_f32 v[38:39], v[38:39], v[204:205]
	v_pk_mul_f32 v[44:45], v[40:41], v[44:45]
	v_pk_mul_f32 v[46:47], v[42:43], v[46:47]
	v_pk_mul_f32 v[36:37], v[32:33], v[36:37]
	v_pk_mul_f32 v[38:39], v[34:35], v[38:39]
	v_cvt_pk_bf16_f32 v210, v44, v45
	v_cvt_pk_bf16_f32 v211, v46, v47
	v_cvt_pk_bf16_f32 v212, v36, v37
	v_cvt_pk_bf16_f32 v213, v38, v39
	global_store_dwordx4 v[216:217], v[210:213], off offset:-2048
	v_pk_fma_f32 v[28:29], v[28:29], v[162:163], v[96:97] op_sel_hi:[1,0,1]
	v_pk_fma_f32 v[30:31], v[30:31], v[162:163], v[98:99] op_sel_hi:[1,0,1]
	v_pk_fma_f32 v[20:21], v[20:21], v[162:163], v[80:81] op_sel_hi:[1,0,1]
	v_pk_fma_f32 v[22:23], v[22:23], v[162:163], v[82:83] op_sel_hi:[1,0,1]
	v_pk_mul_f32 v[198:199], v[28:29], v[222:223] op_sel_hi:[1,0]
	v_pk_mul_f32 v[200:201], v[30:31], v[222:223] op_sel_hi:[1,0]
	v_pk_mul_f32 v[202:203], v[20:21], v[222:223] op_sel_hi:[1,0]
	v_pk_mul_f32 v[204:205], v[22:23], v[222:223] op_sel_hi:[1,0]
	v_pk_fma_f32 v[24:25], v[24:25], v[162:163], v[100:101] op_sel_hi:[1,0,1]
	v_pk_fma_f32 v[26:27], v[26:27], v[162:163], v[102:103] op_sel_hi:[1,0,1]
	v_pk_fma_f32 v[16:17], v[16:17], v[162:163], v[84:85] op_sel_hi:[1,0,1]
	v_pk_fma_f32 v[18:19], v[18:19], v[162:163], v[86:87] op_sel_hi:[1,0,1]
	v_exp_f32_e32 v198, v198
	v_exp_f32_e32 v199, v199
	v_exp_f32_e32 v200, v200
	v_exp_f32_e32 v201, v201
	v_exp_f32_e32 v202, v202
	v_exp_f32_e32 v203, v203
	v_exp_f32_e32 v204, v204
	v_exp_f32_e32 v205, v205
	v_pk_add_f32 v[198:199], v[198:199], v[224:225] op_sel_hi:[1,0]
	v_pk_add_f32 v[200:201], v[200:201], v[224:225] op_sel_hi:[1,0]
	v_pk_add_f32 v[202:203], v[202:203], v[224:225] op_sel_hi:[1,0]
	v_pk_add_f32 v[204:205], v[204:205], v[224:225] op_sel_hi:[1,0]
	v_rcp_f32_e32 v198, v198
	v_rcp_f32_e32 v199, v199
	v_rcp_f32_e32 v200, v200
	v_rcp_f32_e32 v201, v201
	v_rcp_f32_e32 v202, v202
	v_rcp_f32_e32 v203, v203
	v_rcp_f32_e32 v204, v204
	v_rcp_f32_e32 v205, v205
	v_pk_mul_f32 v[28:29], v[28:29], v[198:199]
	v_pk_mul_f32 v[30:31], v[30:31], v[200:201]
	v_pk_mul_f32 v[20:21], v[20:21], v[202:203]
	v_pk_mul_f32 v[22:23], v[22:23], v[204:205]
	v_pk_mul_f32 v[28:29], v[24:25], v[28:29]
	v_pk_mul_f32 v[30:31], v[26:27], v[30:31]
	v_pk_mul_f32 v[20:21], v[16:17], v[20:21]
	v_pk_mul_f32 v[22:23], v[18:19], v[22:23]
	v_cvt_pk_bf16_f32 v206, v28, v29
	v_cvt_pk_bf16_f32 v207, v30, v31
	v_cvt_pk_bf16_f32 v208, v20, v21
	v_cvt_pk_bf16_f32 v209, v22, v23
	global_store_dwordx4 v[216:217], v[206:209], off
	v_pk_fma_f32 v[12:13], v[12:13], v[162:163], v[96:97] op_sel:[0,1,0]
	v_pk_fma_f32 v[14:15], v[14:15], v[162:163], v[98:99] op_sel:[0,1,0]
	v_pk_fma_f32 v[4:5], v[4:5], v[162:163], v[80:81] op_sel:[0,1,0]
	v_pk_fma_f32 v[6:7], v[6:7], v[162:163], v[82:83] op_sel:[0,1,0]
	v_pk_mul_f32 v[198:199], v[12:13], v[222:223] op_sel_hi:[1,0]
	v_pk_mul_f32 v[200:201], v[14:15], v[222:223] op_sel_hi:[1,0]
	v_pk_mul_f32 v[202:203], v[4:5], v[222:223] op_sel_hi:[1,0]
	v_pk_mul_f32 v[204:205], v[6:7], v[222:223] op_sel_hi:[1,0]
	v_pk_fma_f32 v[8:9], v[8:9], v[162:163], v[100:101] op_sel:[0,1,0]
	v_pk_fma_f32 v[10:11], v[10:11], v[162:163], v[102:103] op_sel:[0,1,0]
	v_pk_fma_f32 v[0:1], v[0:1], v[162:163], v[84:85] op_sel:[0,1,0]
	v_pk_fma_f32 v[2:3], v[2:3], v[162:163], v[86:87] op_sel:[0,1,0]
	v_exp_f32_e32 v198, v198
	v_exp_f32_e32 v199, v199
	v_exp_f32_e32 v200, v200
	v_exp_f32_e32 v201, v201
	v_exp_f32_e32 v202, v202
	v_exp_f32_e32 v203, v203
	v_exp_f32_e32 v204, v204
	v_exp_f32_e32 v205, v205
	v_pk_add_f32 v[198:199], v[198:199], v[224:225] op_sel_hi:[1,0]
	v_pk_add_f32 v[200:201], v[200:201], v[224:225] op_sel_hi:[1,0]
	v_pk_add_f32 v[202:203], v[202:203], v[224:225] op_sel_hi:[1,0]
	v_pk_add_f32 v[204:205], v[204:205], v[224:225] op_sel_hi:[1,0]
	v_rcp_f32_e32 v198, v198
	v_rcp_f32_e32 v199, v199
	v_rcp_f32_e32 v200, v200
	v_rcp_f32_e32 v201, v201
	v_rcp_f32_e32 v202, v202
	v_rcp_f32_e32 v203, v203
	v_rcp_f32_e32 v204, v204
	v_rcp_f32_e32 v205, v205
	v_pk_mul_f32 v[12:13], v[12:13], v[198:199]
	v_pk_mul_f32 v[14:15], v[14:15], v[200:201]
	v_pk_mul_f32 v[4:5], v[4:5], v[202:203]
	v_pk_mul_f32 v[6:7], v[6:7], v[204:205]
	v_pk_mul_f32 v[12:13], v[8:9], v[12:13]
	v_pk_mul_f32 v[14:15], v[10:11], v[14:15]
	v_pk_mul_f32 v[4:5], v[0:1], v[4:5]
	v_pk_mul_f32 v[6:7], v[2:3], v[6:7]
	v_cvt_pk_bf16_f32 v210, v12, v13
	v_cvt_pk_bf16_f32 v211, v14, v15
	v_cvt_pk_bf16_f32 v212, v4, v5
	v_cvt_pk_bf16_f32 v213, v6, v7
	global_store_dwordx4 v[216:217], v[210:213], off offset:2048
	s_andn2_b64 vcc, exec, s[2:3]
	s_cbranch_vccnz .LBB0_242
	s_andn2_b64 vcc, exec, s[4:5]
	s_cbranch_vccnz .LBB0_241
	s_barrier
	s_branch .LBB0_241
